# PEER expert phase: static s_setprio 2 for waves 4-7 (SIMD partners of waves 0-3) over the per-wave expert loop, reset at phase end
# speedup vs baseline: 1.0011x; 1.0011x over previous
; #define GAS __attribute__((address_space(1)))
; #define LAS __attribute__((address_space(3)))
; __device__ __forceinline__ float frsq(float x) { return __builtin_amdgcn_rsqf(x); }
; __device__ __forceinline__ void expert_phase(const Frame& F, int l, int xcc, LAS unsigned char* wl, const LAS unsigned char* zb) {
;     ...
;     for (int tb = F.gw; tb < T; tb += 8 * F.ngw) {
;         auto tok = [&](int k) { const int t = tb + k * F.ngw; return t < T ? t : tb; };
;         auto slice_of = [&](int i) { return ((i >> 3) + xcc) & 7; };
;         {
;             float zf = 0.f; asm volatile("" : "+v"(zf)); const f32x4 z = (f32x4){zf, zf, zf, zf};
; #pragma unroll
;             for (int i = 0; i < 8; ++i) *(LAS f32x4*)(SA + (i * 64 + lane) * 4) = z;
; #pragma unroll
;             for (int i = 0; i < 2; ++i) *(LAS f32x4*)(SQ + (i * 64 + lane) * 4) = z;
; #pragma unroll
;             for (int k = 0; k < 8; ++k) { const u32x2 e2 = ldo_u2(EXPI + (size_t)tok(k) * 128, 8u * lane); *(LAS unsigned*)(IDL + k * 256 + lane * 4) = e2.x | (e2.y << 16); }
;             const float* SS2 = (const float*)(F.ws + WS_SS2);
;             float ss[8];
; #pragma unroll
;             for (int k = 0; k < 8; ++k) ss[k] = *(const GAS float*)(SS2 + (size_t)(lane & 31) * T + tok(k));
; #pragma unroll
;             for (int k = 0; k < 8; ++k) { const float tot = wave_sum(ss[k]) * 0.5f; if (lane == 0) RS[k] = frsq(tot * (1.f / D) + EPS); }
.LBB0_1124:
	s_waitcnt lgkmcnt(0)
	v_readlane_b32 s0, v251, 18
	s_add_i32 s26, s26, s0
	s_cmpk_lt_i32 s26, 0x4000
	s_cbranch_scc0 .LBB0_1266
.LBB0_1125:
	v_readfirstlane_b32 s100, v212
	s_cmp_lt_u32 s100, 0x100
	s_cbranch_scc1 .Lp8_prio_0
	s_setprio 2
.Lp8_prio_0:
	v_mov_b32_e32 v0, v185
	s_ashr_i32 s27, s26, 31
	v_add_u32_e32 v4, s83, v182
	s_waitcnt lgkmcnt(0)
	v_mov_b32_e32 v1, v0
	v_mov_b32_e32 v2, v0
	v_mov_b32_e32 v3, v0
	s_lshl_b64 s[2:3], s[26:27], 9
	ds_write_b128 v4, v[0:3]
	ds_write_b128 v4, v[0:3] offset:1024
	ds_write_b128 v4, v[0:3] offset:2048
	ds_write_b128 v4, v[0:3] offset:3072
	ds_write_b128 v4, v[0:3] offset:4096
	ds_write_b128 v4, v[0:3] offset:5120
	ds_write_b128 v4, v[0:3] offset:6144
	ds_write_b128 v4, v[0:3] offset:7168
	ds_write_b128 v4, v[0:3] offset:8192
	ds_write_b128 v4, v[0:3] offset:9216
	v_lshl_add_u64 v[0:1], v[168:169], 0, s[2:3]
	global_load_dwordx2 v[10:11], v[0:1], off
	s_add_i32 s0, s26, s82
	s_cmpk_lt_i32 s0, 0x4000
	s_cselect_b32 s88, s0, s26
	s_ashr_i32 s89, s88, 31
	s_lshl_b64 s[86:87], s[88:89], 9
	s_add_i32 s4, s0, s82
	s_cmpk_lt_i32 s4, 0x4000
	s_cselect_b32 s0, s4, s26
	s_ashr_i32 s1, s0, 31
	v_add_u32_e32 v3, 64, v201
	s_lshl_b64 s[68:69], s[0:1], 9
	s_add_i32 s4, s4, s82
	s_cmpk_lt_i32 s4, 0x4000
	s_cselect_b32 s16, s4, s26
	s_ashr_i32 s17, s16, 31
	s_lshl_b64 s[80:81], s[16:17], 9
	s_add_i32 s4, s4, s82
	s_cmpk_lt_i32 s4, 0x4000
	s_cselect_b32 s14, s4, s26
	s_ashr_i32 s15, s14, 31
	s_lshl_b64 s[8:9], s[14:15], 9
	s_add_i32 s4, s4, s82
	s_cmpk_lt_i32 s4, 0x4000
	s_cselect_b32 s12, s4, s26
	s_ashr_i32 s13, s12, 31
	s_lshl_b64 s[66:67], s[12:13], 9
	s_add_i32 s4, s4, s82
	s_cmpk_lt_i32 s4, 0x4000
	s_cselect_b32 s94, s4, s26
	s_ashr_i32 s95, s94, 31
	s_lshl_b64 s[30:31], s[94:95], 9
	s_add_i32 s4, s4, s82
	s_cmpk_lt_i32 s4, 0x4000
	s_cselect_b32 s6, s4, s26
	s_ashr_i32 s7, s6, 31
	s_lshl_b64 s[44:45], s[6:7], 9
	v_lshl_add_u64 v[8:9], s[6:7], 2, v[166:167]
	v_lshl_add_u64 v[0:1], v[168:169], 0, s[86:87]
	global_load_dwordx2 v[12:13], v[0:1], off
	v_lshl_add_u64 v[0:1], v[168:169], 0, s[68:69]
	global_load_dwordx2 v[14:15], v[0:1], off
	v_lshl_add_u64 v[0:1], v[168:169], 0, s[80:81]
	global_load_dwordx2 v[16:17], v[0:1], off
	v_lshl_add_u64 v[0:1], v[168:169], 0, s[8:9]
	global_load_dwordx2 v[18:19], v[0:1], off
	v_lshl_add_u64 v[0:1], v[168:169], 0, s[66:67]
	global_load_dwordx2 v[20:21], v[0:1], off
	v_lshl_add_u64 v[0:1], v[168:169], 0, s[30:31]
	global_load_dwordx2 v[22:23], v[0:1], off
	v_lshl_add_u64 v[0:1], v[168:169], 0, s[44:45]
	global_load_dwordx2 v[24:25], v[0:1], off
	s_waitcnt vmcnt(0)
	v_lshl_or_b32 v2, v11, 16, v10
	v_lshl_or_b32 v0, v13, 16, v12
	ds_write2st64_b32 v3, v2, v0 offset0:42 offset1:43
	v_lshl_or_b32 v2, v15, 16, v14
	v_lshl_or_b32 v0, v17, 16, v16
	ds_write2st64_b32 v3, v2, v0 offset0:44 offset1:45
	v_lshl_or_b32 v2, v19, 16, v18
	v_lshl_or_b32 v0, v21, 16, v20
	ds_write2st64_b32 v3, v2, v0 offset0:46 offset1:47
	v_lshl_or_b32 v2, v23, 16, v22
	v_lshl_or_b32 v0, v25, 16, v24
	ds_write2st64_b32 v3, v2, v0 offset0:48 offset1:49
	v_lshl_add_u64 v[0:1], s[26:27], 2, v[166:167]
	global_load_dword v7, v[0:1], off
	v_lshl_add_u64 v[0:1], s[88:89], 2, v[166:167]
	global_load_dword v6, v[0:1], off
	v_lshl_add_u64 v[0:1], s[0:1], 2, v[166:167]
	global_load_dword v5, v[0:1], off
	v_lshl_add_u64 v[0:1], s[16:17], 2, v[166:167]
	global_load_dword v4, v[0:1], off
	v_lshl_add_u64 v[0:1], s[14:15], 2, v[166:167]
	global_load_dword v3, v[0:1], off
	v_lshl_add_u64 v[0:1], s[12:13], 2, v[166:167]
	global_load_dword v2, v[0:1], off
	v_lshl_add_u64 v[0:1], s[94:95], 2, v[166:167]
	global_load_dword v1, v[0:1], off
	s_nop 0
	global_load_dword v0, v[8:9], off
	s_waitcnt vmcnt(7)
	s_waitcnt lgkmcnt(0)
	s_nop 1
	v_add_f32_dpp v7, v7, v7 quad_perm:[1,0,3,2] row_mask:0xf bank_mask:0xf
	s_nop 1
	v_add_f32_dpp v7, v7, v7 quad_perm:[2,3,0,1] row_mask:0xf bank_mask:0xf
	s_nop 1
	v_add_f32_dpp v7, v7, v7 row_half_mirror row_mask:0xf bank_mask:0xf
	s_nop 1
	v_add_f32_dpp v7, v7, v7 row_mirror row_mask:0xf bank_mask:0xf
	s_nop 1
	v_add_f32_dpp v7, v7, v7 row_bcast:15 row_mask:0xa bank_mask:0xf
	s_nop 1
	v_add_f32_dpp v7, v7, v7 row_bcast:31 row_mask:0xc bank_mask:0xf
	s_nop 1
	v_readlane_b32 s100, v7, 63
	s_nop 3
	v_mov_b32_e32 v7, s100
	v_mov_b32_e32 v8, 0
	s_and_saveexec_b64 s[64:65], s[34:35]
	s_cbranch_execz .LBB0_1127
	s_waitcnt lgkmcnt(0)
	v_add_f32_e32 v7, v7, v8
	v_mul_f32_e32 v7, 0.5, v7
	v_fmamk_f32 v7, v7, 0x3a000000, v214
	v_rsq_f32_e32 v7, v7
	v_mov_b32_e32 v8, s83
	ds_write_b32 v8, v7 offset:10240

; __device__ __forceinline__ unsigned xb_xcc_id() { return (unsigned)__builtin_amdgcn_s_getreg((3 << 11) | 20) & 0xFu; }
; #define SEAM(k) do { if (IN((k) + 1)) xcd_barrier(bar, F.wave); } while (0)
; __global__ void __launch_bounds__(NWAVES * 64, 2) hybrid_fwd(Args args) {
;     ...
;             expert_phase(F, l, (int)xb_xcc_id(), wl, zb);
;             SEAM(pb + 7);
.LBB0_1266:
	s_setprio 0
	v_readlane_b32 s80, v250, 18
	v_readlane_b32 s88, v250, 20
	v_readlane_b32 s56, v250, 22
	v_readlane_b32 s64, v250, 26
	v_readlane_b32 s30, v250, 28
	v_readlane_b32 s40, v250, 32
	v_readlane_b32 s86, v250, 34
	v_readlane_b32 s87, v250, 35
	v_readlane_b32 s69, v252, 22
	v_readlane_b32 s70, v252, 23
	v_readlane_b32 s94, v250, 15
	v_readlane_b32 s67, v250, 17
	v_readlane_b32 s81, v250, 19
	v_readlane_b32 s89, v250, 21
	v_readlane_b32 s57, v250, 23
	v_readlane_b32 s58, v250, 24
	v_readlane_b32 s68, v250, 25
	v_readlane_b32 s65, v250, 27
	v_readlane_b32 s31, v250, 29
	v_readlane_b32 s66, v250, 30
	v_readlane_b32 s25, v250, 31
	v_readlane_b32 s41, v250, 33
	s_movk_i32 s33, 0x1100
	s_mov_b64 s[22:23], 0x800
	v_readlane_b32 s95, v250, 16
